# layer-0 MFMAs of the first two batch tiles start right after the first lane swap; second swap and operand patch run under them
# speedup vs baseline: 1.0028x; 1.0028x over previous
.LBB1_4:
	s_and_saveexec_b64 s[8:9], s[2:3]
	v_perm_b32 v5, v1, v102, s23
	v_perm_b32 v9, v121, v103, s23
	s_or_b64 exec, exec, s[8:9]
	v_mov_b32_e32 v144, v1
	v_mov_b32_e32 v145, v121
	v_mfma_f32_16x16x32_f16 v[164:167], v[30:33], v[2:5], 0
	v_mfma_f32_16x16x32_f16 v[180:183], v[22:25], v[2:5], 0
	s_cmp_lg_u32 s22, 0x818000
	v_permlane32_swap_b32_e32 v1, v144
	v_permlane32_swap_b32_e32 v121, v145
	v_mfma_f32_16x16x32_f16 v[168:171], v[30:33], v[6:9], 0
	v_mfma_f32_16x16x32_f16 v[184:187], v[22:25], v[6:9], 0
	s_cselect_b32 s9, s11, 15
	s_and_saveexec_b64 s[32:33], s[2:3]
	v_perm_b32 v17, v144, v115, s23
	v_perm_b32 v29, v145, v116, s23
	s_or_b64 exec, exec, s[32:33]
	v_mfma_f32_16x16x32_f16 v[172:175], v[30:33], v[14:17], 0
	v_mfma_f32_16x16x32_f16 v[188:191], v[22:25], v[14:17], 0
	v_mfma_f32_16x16x32_f16 v[176:179], v[30:33], v[26:29], 0
	v_mfma_f32_16x16x32_f16 v[192:195], v[22:25], v[26:29], 0
	v_mfma_f32_16x16x32_f16 v[208:211], v[18:21], v[2:5], 0
	v_mfma_f32_16x16x32_f16 v[224:227], v[10:13], v[2:5], 0
	v_cvt_pk_f16_f32 v122, v164, v165
	v_cvt_pk_f16_f32 v123, v166, v167
	v_pk_max_f16 v122, v122, 0
	v_pk_max_f16 v123, v123, 0
	v_cvt_pk_f16_f32 v124, v180, v181
	v_cvt_pk_f16_f32 v125, v182, v183
	v_pk_max_f16 v124, v124, 0
	v_pk_max_f16 v125, v125, 0
	ds_write_b128 v107, v[122:125]
	v_mfma_f32_16x16x32_f16 v[212:215], v[18:21], v[6:9], 0
	v_mfma_f32_16x16x32_f16 v[228:231], v[10:13], v[6:9], 0
	v_cvt_pk_f16_f32 v126, v168, v169
	v_cvt_pk_f16_f32 v127, v170, v171
	v_pk_max_f16 v126, v126, 0
	v_pk_max_f16 v127, v127, 0
	v_cvt_pk_f16_f32 v128, v184, v185
	v_cvt_pk_f16_f32 v129, v186, v187
	v_pk_max_f16 v128, v128, 0
	v_pk_max_f16 v129, v129, 0
	ds_write_b128 v107, v[126:129] offset:16384
	v_mfma_f32_16x16x32_f16 v[216:219], v[18:21], v[14:17], 0
	v_mfma_f32_16x16x32_f16 v[232:235], v[10:13], v[14:17], 0
	v_cvt_pk_f16_f32 v134, v172, v173
	v_cvt_pk_f16_f32 v135, v174, v175
	v_pk_max_f16 v134, v134, 0
	v_pk_max_f16 v135, v135, 0
	v_cvt_pk_f16_f32 v136, v188, v189
	v_cvt_pk_f16_f32 v137, v190, v191
	v_pk_max_f16 v136, v136, 0
	v_pk_max_f16 v137, v137, 0
	ds_write_b128 v107, v[134:137] offset:32768
	v_mfma_f32_16x16x32_f16 v[220:223], v[18:21], v[26:29], 0
	v_mfma_f32_16x16x32_f16 v[236:239], v[10:13], v[26:29], 0
	v_cvt_pk_f16_f32 v138, v176, v177
	v_cvt_pk_f16_f32 v139, v178, v179
	v_pk_max_f16 v138, v138, 0
	v_pk_max_f16 v139, v139, 0
	v_cvt_pk_f16_f32 v140, v192, v193
	v_cvt_pk_f16_f32 v141, v194, v195
	v_pk_max_f16 v140, v140, 0
	v_pk_max_f16 v141, v141, 0
	ds_write_b128 v107, v[138:141] offset:49152
	v_add_u32_e32 v111, s64, v111
	v_add_u32_e32 v98, s65, v98
	s_lshl_b32 s20, s9, 7
	v_lshl_add_u64 v[0:1], s[20:21], 3, v[132:133]
	s_add_i32 s25, s22, s34
	s_lshl_b32 s8, s9, 8
	buffer_load_dwordx4 v[192:195], v147, s[16:19], s25 offen
	buffer_load_dwordx4 v[196:199], v148, s[16:19], s25 offen
	buffer_load_dwordx4 v[200:203], v149, s[16:19], s25 offen
	buffer_load_dwordx4 v[204:207], v150, s[16:19], s25 offen
	s_waitcnt vmcnt(19)
	v_mfma_f32_16x16x32_f16 v[164:167], v[58:61], v[122:125], v[240:243]
	v_cvt_pk_f16_f32 v142, v208, v209
	v_cvt_pk_f16_f32 v143, v210, v211
	v_mfma_f32_16x16x32_f16 v[168:171], v[58:61], v[126:129], v[240:243]
	v_pk_max_f16 v142, v142, 0
	v_pk_max_f16 v143, v143, 0
	v_mfma_f32_16x16x32_f16 v[172:175], v[58:61], v[134:137], v[240:243]
	v_cvt_pk_f16_f32 v144, v224, v225
	v_cvt_pk_f16_f32 v145, v226, v227
	v_mfma_f32_16x16x32_f16 v[10:13], v[58:61], v[138:141], v[240:243]
	v_pk_max_f16 v144, v144, 0
	v_pk_max_f16 v145, v145, 0
	ds_write_b128 v108, v[142:145]
	s_waitcnt vmcnt(18)
	v_mfma_f32_16x16x32_f16 v[58:61], v[54:57], v[122:125], v[244:247]
	v_cvt_pk_f16_f32 v152, v212, v213
	v_cvt_pk_f16_f32 v153, v214, v215
	v_mfma_f32_16x16x32_f16 v[176:179], v[54:57], v[126:129], v[244:247]
	v_pk_max_f16 v152, v152, 0
	v_pk_max_f16 v153, v153, 0
	v_mfma_f32_16x16x32_f16 v[180:183], v[54:57], v[134:137], v[244:247]
	v_cvt_pk_f16_f32 v154, v228, v229
	v_cvt_pk_f16_f32 v155, v230, v231
	v_mfma_f32_16x16x32_f16 v[18:21], v[54:57], v[138:141], v[244:247]
	v_pk_max_f16 v154, v154, 0
	v_pk_max_f16 v155, v155, 0
	ds_write_b128 v108, v[152:155] offset:16384
	s_waitcnt vmcnt(17)
	v_mfma_f32_16x16x32_f16 v[54:57], v[50:53], v[122:125], v[248:251]
	v_cvt_pk_f16_f32 v156, v216, v217
	v_cvt_pk_f16_f32 v157, v218, v219
	v_mfma_f32_16x16x32_f16 v[184:187], v[50:53], v[126:129], v[248:251]
	v_pk_max_f16 v156, v156, 0
	v_pk_max_f16 v157, v157, 0
	v_mfma_f32_16x16x32_f16 v[188:191], v[50:53], v[134:137], v[248:251]
	v_cvt_pk_f16_f32 v158, v232, v233
	v_cvt_pk_f16_f32 v159, v234, v235
	v_mfma_f32_16x16x32_f16 v[22:25], v[50:53], v[138:141], v[248:251]
	v_pk_max_f16 v158, v158, 0
	v_pk_max_f16 v159, v159, 0
	ds_write_b128 v108, v[156:159] offset:32768
	s_waitcnt vmcnt(16)
	v_mfma_f32_16x16x32_f16 v[50:53], v[38:41], v[122:125], v[252:255]
	v_cvt_pk_f16_f32 v160, v220, v221
	v_cvt_pk_f16_f32 v161, v222, v223
	v_mfma_f32_16x16x32_f16 v[122:125], v[38:41], v[126:129], v[252:255]
	v_pk_max_f16 v160, v160, 0
	v_pk_max_f16 v161, v161, 0
	v_mfma_f32_16x16x32_f16 v[126:129], v[38:41], v[134:137], v[252:255]
	v_cvt_pk_f16_f32 v162, v236, v237
	v_cvt_pk_f16_f32 v163, v238, v239
	v_mfma_f32_16x16x32_f16 v[38:41], v[38:41], v[138:141], v[252:255]
	v_pk_max_f16 v162, v162, 0
	v_pk_max_f16 v163, v163, 0
	ds_write_b128 v108, v[160:163] offset:49152
	s_add_i32 s9, s22, s35
	s_waitcnt vmcnt(15)
	v_mfma_f32_16x16x32_f16 v[164:167], v[94:97], v[142:145], v[164:167]
	v_mfma_f32_16x16x32_f16 v[168:171], v[94:97], v[152:155], v[168:171]
	s_waitcnt vmcnt(14)
	v_mfma_f32_16x16x32_f16 v[58:61], v[90:93], v[142:145], v[58:61]
	v_mfma_f32_16x16x32_f16 v[176:179], v[90:93], v[152:155], v[176:179]
	s_waitcnt vmcnt(13)
	v_mfma_f32_16x16x32_f16 v[54:57], v[78:81], v[142:145], v[54:57]
	v_mfma_f32_16x16x32_f16 v[184:187], v[78:81], v[152:155], v[184:187]
	s_waitcnt vmcnt(12)
	v_mfma_f32_16x16x32_f16 v[50:53], v[34:37], v[142:145], v[50:53]
	buffer_load_dwordx4 v[140:143], v147, s[16:19], s9 offen
	buffer_load_dwordx4 v[220:223], v148, s[16:19], s9 offen
	v_mfma_f32_16x16x32_f16 v[122:125], v[34:37], v[152:155], v[122:125]
	buffer_load_dwordx4 v[152:155], v149, s[16:19], s9 offen
	buffer_load_dwordx4 v[224:227], v150, s[16:19], s9 offen
	s_mov_b32 s9, s21
	s_waitcnt lgkmcnt(0)
	s_barrier
	v_add_u32_e32 v99, s66, v99
	ds_read_b128 v[136:139], v99
	ds_read_b128 v[208:211], v99 offset:16384
	ds_read_b128 v[212:215], v99 offset:32768
	ds_read_b128 v[216:219], v99 offset:49152
	v_mfma_f32_16x16x32_f16 v[172:175], v[94:97], v[156:159], v[172:175]
	v_mfma_f32_16x16x32_f16 v[94:97], v[94:97], v[160:163], v[10:13]
	s_nop 2
	v_lshl_add_u64 v[10:11], s[8:9], 4, v[130:131]
	v_mfma_f32_16x16x32_f16 v[180:183], v[90:93], v[156:159], v[180:183]
	v_mfma_f32_16x16x32_f16 v[90:93], v[90:93], v[160:163], v[18:21]
	v_mfma_f32_16x16x32_f16 v[188:191], v[78:81], v[156:159], v[188:191]
	v_mfma_f32_16x16x32_f16 v[78:81], v[78:81], v[160:163], v[22:25]
	global_load_dwordx4 v[30:33], v[10:11], off
	s_nop 1
	global_load_dwordx4 v[22:25], v[10:11], off offset:1024
	global_load_dwordx4 v[18:21], v[10:11], off offset:2048
	s_nop 0
	global_load_dwordx4 v[10:13], v[10:11], off offset:3072
	s_nop 0
	global_load_dwordx2 v[134:135], v[0:1], off
	v_mfma_f32_16x16x32_f16 v[126:129], v[34:37], v[156:159], v[126:129]
	v_mfma_f32_16x16x32_f16 v[34:37], v[34:37], v[160:163], v[38:41]
	s_nop 2
	v_add_u32_e32 v100, s67, v100
	ds_read_b128 v[38:41], v100
	ds_read_b128 v[156:159], v100 offset:16384
	ds_read_b128 v[160:163], v100 offset:32768
	ds_read_b128 v[228:231], v100 offset:49152
	s_add_i32 s8, s22, s36
	s_waitcnt vmcnt(20) lgkmcnt(7)
	v_mfma_f32_16x16x32_f16 v[164:167], v[82:85], v[136:139], v[164:167]
	s_waitcnt lgkmcnt(6)
	v_mfma_f32_16x16x32_f16 v[168:171], v[82:85], v[208:211], v[168:171]
	s_waitcnt lgkmcnt(5)
	v_mfma_f32_16x16x32_f16 v[172:175], v[82:85], v[212:215], v[172:175]
	s_waitcnt lgkmcnt(4)
	v_mfma_f32_16x16x32_f16 v[82:85], v[82:85], v[216:219], v[94:97]
	s_waitcnt vmcnt(19)
	v_mfma_f32_16x16x32_f16 v[58:61], v[70:73], v[136:139], v[58:61]
	v_mfma_f32_16x16x32_f16 v[94:97], v[70:73], v[208:211], v[176:179]
	v_mfma_f32_16x16x32_f16 v[176:179], v[70:73], v[212:215], v[180:183]
	v_mfma_f32_16x16x32_f16 v[70:73], v[70:73], v[216:219], v[90:93]
	s_waitcnt vmcnt(18)
	v_mfma_f32_16x16x32_f16 v[54:57], v[62:65], v[136:139], v[54:57]
	v_mfma_f32_16x16x32_f16 v[90:93], v[62:65], v[208:211], v[184:187]
	v_mfma_f32_16x16x32_f16 v[180:183], v[62:65], v[212:215], v[188:191]
	v_mfma_f32_16x16x32_f16 v[62:65], v[62:65], v[216:219], v[78:81]
	s_waitcnt vmcnt(17)
	v_mfma_f32_16x16x32_f16 v[50:53], v[42:45], v[136:139], v[50:53]
	v_mfma_f32_16x16x32_f16 v[78:81], v[42:45], v[208:211], v[122:125]
	v_mfma_f32_16x16x32_f16 v[122:125], v[42:45], v[212:215], v[126:129]
	s_nop 2
	buffer_load_dwordx4 v[126:129], v147, s[16:19], s8 offen
	buffer_load_dwordx4 v[136:139], v148, s[16:19], s8 offen
	buffer_load_dwordx4 v[184:187], v149, s[16:19], s8 offen
	buffer_load_dwordx4 v[188:191], v150, s[16:19], s8 offen
	v_mfma_f32_16x16x32_f16 v[34:37], v[42:45], v[216:219], v[34:37]
	v_add_u32_e32 v111, s68, v111
	ds_read_b128 v[42:45], v111
	ds_read_b128 v[208:211], v111 offset:16384
	ds_read_b128 v[212:215], v111 offset:32768
	ds_read_b128 v[216:219], v111 offset:49152
	s_add_i32 s8, s22, s37
	s_waitcnt vmcnt(20) lgkmcnt(7)
	v_mfma_f32_16x16x32_f16 v[164:167], v[86:89], v[38:41], v[164:167]
	s_waitcnt lgkmcnt(6)
	v_mfma_f32_16x16x32_f16 v[168:171], v[86:89], v[156:159], v[168:171]
	s_waitcnt lgkmcnt(5)
	v_mfma_f32_16x16x32_f16 v[172:175], v[86:89], v[160:163], v[172:175]
	s_waitcnt lgkmcnt(4)
	v_mfma_f32_16x16x32_f16 v[82:85], v[86:89], v[228:231], v[82:85]
	s_waitcnt vmcnt(19)
	v_mfma_f32_16x16x32_f16 v[58:61], v[74:77], v[38:41], v[58:61]
	v_mfma_f32_16x16x32_f16 v[86:89], v[74:77], v[156:159], v[94:97]
	v_mfma_f32_16x16x32_f16 v[94:97], v[74:77], v[160:163], v[176:179]
	v_mfma_f32_16x16x32_f16 v[70:73], v[74:77], v[228:231], v[70:73]
	s_waitcnt vmcnt(18)
	v_mfma_f32_16x16x32_f16 v[54:57], v[66:69], v[38:41], v[54:57]
	v_mfma_f32_16x16x32_f16 v[74:77], v[66:69], v[156:159], v[90:93]
	v_mfma_f32_16x16x32_f16 v[90:93], v[66:69], v[160:163], v[180:183]
	v_mfma_f32_16x16x32_f16 v[62:65], v[66:69], v[228:231], v[62:65]
	s_waitcnt vmcnt(17)
	v_mfma_f32_16x16x32_f16 v[38:41], v[46:49], v[38:41], v[50:53]
	v_mfma_f32_16x16x32_f16 v[50:53], v[46:49], v[156:159], v[78:81]
	v_mfma_f32_16x16x32_f16 v[66:69], v[46:49], v[160:163], v[122:125]
	s_nop 1
	buffer_load_dwordx4 v[78:81], v147, s[16:19], s8 offen
	buffer_load_dwordx4 v[122:125], v148, s[16:19], s8 offen
	buffer_load_dwordx4 v[156:159], v149, s[16:19], s8 offen
	buffer_load_dwordx4 v[160:163], v150, s[16:19], s8 offen
	v_mfma_f32_16x16x32_f16 v[34:37], v[46:49], v[228:231], v[34:37]
	v_add_u32_e32 v98, s69, v98
	ds_read_b128 v[46:49], v98
	ds_read_b128 v[176:179], v98 offset:16384
	ds_read_b128 v[180:183], v98 offset:32768
	ds_read_b128 v[228:231], v98 offset:49152
	s_add_i32 s8, s22, s38
	s_waitcnt vmcnt(20) lgkmcnt(7)
	v_mfma_f32_16x16x32_f16 v[164:167], v[192:195], v[42:45], v[164:167]
	s_waitcnt lgkmcnt(6)
	v_mfma_f32_16x16x32_f16 v[168:171], v[192:195], v[208:211], v[168:171]
	s_waitcnt lgkmcnt(5)
	v_mfma_f32_16x16x32_f16 v[172:175], v[192:195], v[212:215], v[172:175]
	s_waitcnt lgkmcnt(4)
	v_mfma_f32_16x16x32_f16 v[82:85], v[192:195], v[216:219], v[82:85]
	s_waitcnt vmcnt(19)
	v_mfma_f32_16x16x32_f16 v[58:61], v[196:199], v[42:45], v[58:61]
	v_mfma_f32_16x16x32_f16 v[86:89], v[196:199], v[208:211], v[86:89]
	v_mfma_f32_16x16x32_f16 v[94:97], v[196:199], v[212:215], v[94:97]
	v_mfma_f32_16x16x32_f16 v[70:73], v[196:199], v[216:219], v[70:73]
	s_waitcnt vmcnt(18)
	v_mfma_f32_16x16x32_f16 v[54:57], v[200:203], v[42:45], v[54:57]
	v_mfma_f32_16x16x32_f16 v[74:77], v[200:203], v[208:211], v[74:77]
	v_mfma_f32_16x16x32_f16 v[90:93], v[200:203], v[212:215], v[90:93]
	v_mfma_f32_16x16x32_f16 v[62:65], v[200:203], v[216:219], v[62:65]
	s_waitcnt vmcnt(17)
	v_mfma_f32_16x16x32_f16 v[38:41], v[204:207], v[42:45], v[38:41]
	v_mfma_f32_16x16x32_f16 v[42:45], v[204:207], v[208:211], v[50:53]
	v_mfma_f32_16x16x32_f16 v[50:53], v[204:207], v[212:215], v[66:69]
	s_nop 2
	buffer_load_dwordx4 v[66:69], v147, s[16:19], s8 offen
	buffer_load_dwordx4 v[192:195], v148, s[16:19], s8 offen
	buffer_load_dwordx4 v[196:199], v149, s[16:19], s8 offen
	buffer_load_dwordx4 v[200:203], v150, s[16:19], s8 offen
	v_mfma_f32_16x16x32_f16 v[34:37], v[204:207], v[216:219], v[34:37]
	v_add_u32_e32 v99, s70, v99
	ds_read_b128 v[204:207], v99
	ds_read_b128 v[208:211], v99 offset:16384
	ds_read_b128 v[212:215], v99 offset:32768
	ds_read_b128 v[216:219], v99 offset:49152
	s_add_i32 s8, s22, s39
	s_waitcnt vmcnt(20) lgkmcnt(7)
	v_mfma_f32_16x16x32_f16 v[164:167], v[140:143], v[46:49], v[164:167]
	s_waitcnt lgkmcnt(6)
	v_mfma_f32_16x16x32_f16 v[168:171], v[140:143], v[176:179], v[168:171]
	s_waitcnt lgkmcnt(5)
	v_mfma_f32_16x16x32_f16 v[172:175], v[140:143], v[180:183], v[172:175]
	s_waitcnt lgkmcnt(4)
	v_mfma_f32_16x16x32_f16 v[82:85], v[140:143], v[228:231], v[82:85]
	s_waitcnt vmcnt(19)
	v_mfma_f32_16x16x32_f16 v[58:61], v[220:223], v[46:49], v[58:61]
	v_mfma_f32_16x16x32_f16 v[86:89], v[220:223], v[176:179], v[86:89]
	s_waitcnt vmcnt(18)
	v_mfma_f32_16x16x32_f16 v[54:57], v[152:155], v[46:49], v[54:57]
	v_mfma_f32_16x16x32_f16 v[74:77], v[152:155], v[176:179], v[74:77]
	v_mfma_f32_16x16x32_f16 v[90:93], v[152:155], v[180:183], v[90:93]
	v_mfma_f32_16x16x32_f16 v[62:65], v[152:155], v[228:231], v[62:65]
	s_waitcnt vmcnt(17)
	v_mfma_f32_16x16x32_f16 v[38:41], v[224:227], v[46:49], v[38:41]
	v_mfma_f32_16x16x32_f16 v[42:45], v[224:227], v[176:179], v[42:45]
	v_mfma_f32_16x16x32_f16 v[46:49], v[224:227], v[180:183], v[50:53]
	s_nop 2
	buffer_load_dwordx4 v[50:53], v147, s[16:19], s8 offen
	buffer_load_dwordx4 v[140:143], v148, s[16:19], s8 offen
	buffer_load_dwordx4 v[152:155], v149, s[16:19], s8 offen
	buffer_load_dwordx4 v[176:179], v150, s[16:19], s8 offen
	v_mfma_f32_16x16x32_f16 v[94:97], v[220:223], v[180:183], v[94:97]
	v_mfma_f32_16x16x32_f16 v[70:73], v[220:223], v[228:231], v[70:73]
	v_mfma_f32_16x16x32_f16 v[34:37], v[224:227], v[228:231], v[34:37]
	v_add_u32_e32 v100, s71, v100
	ds_read_b128 v[180:183], v100
	ds_read_b128 v[220:223], v100 offset:16384
	ds_read_b128 v[224:227], v100 offset:32768
	ds_read_b128 v[228:231], v100 offset:49152
	s_add_i32 s8, s22, s40
	s_waitcnt vmcnt(15) lgkmcnt(7)
	v_mfma_f32_16x16x32_f16 v[164:167], v[126:129], v[204:207], v[164:167]
	s_waitcnt lgkmcnt(6)
	v_mfma_f32_16x16x32_f16 v[168:171], v[126:129], v[208:211], v[168:171]
	s_waitcnt lgkmcnt(5)
	v_mfma_f32_16x16x32_f16 v[172:175], v[126:129], v[212:215], v[172:175]
	s_waitcnt lgkmcnt(4)
	v_mfma_f32_16x16x32_f16 v[82:85], v[126:129], v[216:219], v[82:85]
	s_waitcnt vmcnt(14)
	v_mfma_f32_16x16x32_f16 v[58:61], v[136:139], v[204:207], v[58:61]
	v_mfma_f32_16x16x32_f16 v[86:89], v[136:139], v[208:211], v[86:89]
	v_mfma_f32_16x16x32_f16 v[94:97], v[136:139], v[212:215], v[94:97]
	v_mfma_f32_16x16x32_f16 v[70:73], v[136:139], v[216:219], v[70:73]
	s_waitcnt vmcnt(13)
	v_mfma_f32_16x16x32_f16 v[54:57], v[184:187], v[204:207], v[54:57]
	v_mfma_f32_16x16x32_f16 v[74:77], v[184:187], v[208:211], v[74:77]
	v_mfma_f32_16x16x32_f16 v[90:93], v[184:187], v[212:215], v[90:93]
	v_mfma_f32_16x16x32_f16 v[62:65], v[184:187], v[216:219], v[62:65]
	s_waitcnt vmcnt(12)
	v_mfma_f32_16x16x32_f16 v[38:41], v[188:191], v[204:207], v[38:41]
	buffer_load_dwordx4 v[126:129], v147, s[16:19], s8 offen
	buffer_load_dwordx4 v[136:139], v148, s[16:19], s8 offen
	buffer_load_dwordx4 v[184:187], v149, s[16:19], s8 offen
	buffer_load_dwordx4 v[204:207], v150, s[16:19], s8 offen
	v_mfma_f32_16x16x32_f16 v[42:45], v[188:191], v[208:211], v[42:45]
	v_mfma_f32_16x16x32_f16 v[46:49], v[188:191], v[212:215], v[46:49]
	v_mfma_f32_16x16x32_f16 v[34:37], v[188:191], v[216:219], v[34:37]
	v_add_u32_e32 v111, s72, v111
	ds_read_b128 v[188:191], v111
	ds_read_b128 v[208:211], v111 offset:16384
	ds_read_b128 v[212:215], v111 offset:32768
	ds_read_b128 v[216:219], v111 offset:49152
	s_add_i32 s8, s22, s41
	s_waitcnt vmcnt(15) lgkmcnt(7)
	v_mfma_f32_16x16x32_f16 v[164:167], v[78:81], v[180:183], v[164:167]
	s_waitcnt lgkmcnt(6)
	v_mfma_f32_16x16x32_f16 v[168:171], v[78:81], v[220:223], v[168:171]
	s_waitcnt lgkmcnt(5)
	v_mfma_f32_16x16x32_f16 v[172:175], v[78:81], v[224:227], v[172:175]
	s_waitcnt lgkmcnt(4)
	v_mfma_f32_16x16x32_f16 v[78:81], v[78:81], v[228:231], v[82:85]
	s_waitcnt vmcnt(14)
	v_mfma_f32_16x16x32_f16 v[58:61], v[122:125], v[180:183], v[58:61]
	v_mfma_f32_16x16x32_f16 v[82:85], v[122:125], v[220:223], v[86:89]
	v_mfma_f32_16x16x32_f16 v[86:89], v[122:125], v[224:227], v[94:97]
	v_mfma_f32_16x16x32_f16 v[70:73], v[122:125], v[228:231], v[70:73]
	s_waitcnt vmcnt(13)
	v_mfma_f32_16x16x32_f16 v[54:57], v[156:159], v[180:183], v[54:57]
	v_mfma_f32_16x16x32_f16 v[74:77], v[156:159], v[220:223], v[74:77]
	v_mfma_f32_16x16x32_f16 v[90:93], v[156:159], v[224:227], v[90:93]
	v_mfma_f32_16x16x32_f16 v[62:65], v[156:159], v[228:231], v[62:65]
	s_waitcnt vmcnt(12)
	v_mfma_f32_16x16x32_f16 v[38:41], v[160:163], v[180:183], v[38:41]
	buffer_load_dwordx4 v[94:97], v147, s[16:19], s8 offen
	buffer_load_dwordx4 v[122:125], v148, s[16:19], s8 offen
	buffer_load_dwordx4 v[156:159], v149, s[16:19], s8 offen
	buffer_load_dwordx4 v[180:183], v150, s[16:19], s8 offen
	v_mfma_f32_16x16x32_f16 v[42:45], v[160:163], v[220:223], v[42:45]
	v_mfma_f32_16x16x32_f16 v[46:49], v[160:163], v[224:227], v[46:49]
	v_mfma_f32_16x16x32_f16 v[34:37], v[160:163], v[228:231], v[34:37]
	v_add_u32_e32 v98, s73, v98
	ds_read_b128 v[160:163], v98
	ds_read_b128 v[220:223], v98 offset:16384
	ds_read_b128 v[224:227], v98 offset:32768
	ds_read_b128 v[228:231], v98 offset:49152
	s_add_i32 s8, s22, s42
	s_waitcnt vmcnt(15) lgkmcnt(7)
	v_mfma_f32_16x16x32_f16 v[164:167], v[66:69], v[188:191], v[164:167]
	s_waitcnt lgkmcnt(6)
	v_mfma_f32_16x16x32_f16 v[168:171], v[66:69], v[208:211], v[168:171]
	s_waitcnt lgkmcnt(5)
	v_mfma_f32_16x16x32_f16 v[172:175], v[66:69], v[212:215], v[172:175]
	s_waitcnt lgkmcnt(4)
	v_mfma_f32_16x16x32_f16 v[66:69], v[66:69], v[216:219], v[78:81]
	s_waitcnt vmcnt(14)
	v_mfma_f32_16x16x32_f16 v[58:61], v[192:195], v[188:191], v[58:61]
	v_mfma_f32_16x16x32_f16 v[78:81], v[192:195], v[208:211], v[82:85]
	v_mfma_f32_16x16x32_f16 v[82:85], v[192:195], v[212:215], v[86:89]
	v_mfma_f32_16x16x32_f16 v[70:73], v[192:195], v[216:219], v[70:73]
	s_waitcnt vmcnt(13)
	v_mfma_f32_16x16x32_f16 v[54:57], v[196:199], v[188:191], v[54:57]
	v_mfma_f32_16x16x32_f16 v[74:77], v[196:199], v[208:211], v[74:77]
	v_mfma_f32_16x16x32_f16 v[86:89], v[196:199], v[212:215], v[90:93]
	v_mfma_f32_16x16x32_f16 v[62:65], v[196:199], v[216:219], v[62:65]
	s_waitcnt vmcnt(12)
	v_mfma_f32_16x16x32_f16 v[38:41], v[200:203], v[188:191], v[38:41]
	buffer_load_dwordx4 v[90:93], v147, s[16:19], s8 offen
	buffer_load_dwordx4 v[188:191], v148, s[16:19], s8 offen
	buffer_load_dwordx4 v[192:195], v149, s[16:19], s8 offen
	buffer_load_dwordx4 v[196:199], v150, s[16:19], s8 offen
	v_mfma_f32_16x16x32_f16 v[42:45], v[200:203], v[208:211], v[42:45]
	v_mfma_f32_16x16x32_f16 v[46:49], v[200:203], v[212:215], v[46:49]
	v_mfma_f32_16x16x32_f16 v[34:37], v[200:203], v[216:219], v[34:37]
	v_add_u32_e32 v99, s74, v99
	ds_read_b128 v[200:203], v99
	ds_read_b128 v[208:211], v99 offset:16384
	ds_read_b128 v[212:215], v99 offset:32768
	ds_read_b128 v[216:219], v99 offset:49152
	s_add_i32 s8, s22, s43
	s_waitcnt vmcnt(15) lgkmcnt(7)
	v_mfma_f32_16x16x32_f16 v[164:167], v[50:53], v[160:163], v[164:167]
	s_waitcnt lgkmcnt(6)
	v_mfma_f32_16x16x32_f16 v[168:171], v[50:53], v[220:223], v[168:171]
	s_waitcnt lgkmcnt(5)
	v_mfma_f32_16x16x32_f16 v[172:175], v[50:53], v[224:227], v[172:175]
	s_waitcnt lgkmcnt(4)
	v_mfma_f32_16x16x32_f16 v[50:53], v[50:53], v[228:231], v[66:69]
	s_waitcnt vmcnt(14)
	v_mfma_f32_16x16x32_f16 v[58:61], v[140:143], v[160:163], v[58:61]
	v_mfma_f32_16x16x32_f16 v[66:69], v[140:143], v[220:223], v[78:81]
	v_mfma_f32_16x16x32_f16 v[78:81], v[140:143], v[224:227], v[82:85]
	v_mfma_f32_16x16x32_f16 v[70:73], v[140:143], v[228:231], v[70:73]
	s_waitcnt vmcnt(13)
	v_mfma_f32_16x16x32_f16 v[54:57], v[152:155], v[160:163], v[54:57]
	v_mfma_f32_16x16x32_f16 v[74:77], v[152:155], v[220:223], v[74:77]
	v_mfma_f32_16x16x32_f16 v[82:85], v[152:155], v[224:227], v[86:89]
	v_mfma_f32_16x16x32_f16 v[62:65], v[152:155], v[228:231], v[62:65]
	s_waitcnt vmcnt(12)
	v_mfma_f32_16x16x32_f16 v[38:41], v[176:179], v[160:163], v[38:41]
	buffer_load_dwordx4 v[86:89], v147, s[16:19], s8 offen
	buffer_load_dwordx4 v[140:143], v148, s[16:19], s8 offen
	buffer_load_dwordx4 v[152:155], v149, s[16:19], s8 offen
	buffer_load_dwordx4 v[160:163], v150, s[16:19], s8 offen
	v_mfma_f32_16x16x32_f16 v[42:45], v[176:179], v[220:223], v[42:45]
	v_mfma_f32_16x16x32_f16 v[46:49], v[176:179], v[224:227], v[46:49]
	v_mfma_f32_16x16x32_f16 v[34:37], v[176:179], v[228:231], v[34:37]
	v_add_u32_e32 v100, s75, v100
	ds_read_b128 v[176:179], v100
	ds_read_b128 v[220:223], v100 offset:16384
	ds_read_b128 v[224:227], v100 offset:32768
	ds_read_b128 v[228:231], v100 offset:49152
	s_add_i32 s8, s22, s44
	s_waitcnt vmcnt(15) lgkmcnt(7)
	v_mfma_f32_16x16x32_f16 v[164:167], v[126:129], v[200:203], v[164:167]
	s_waitcnt lgkmcnt(6)
	v_mfma_f32_16x16x32_f16 v[168:171], v[126:129], v[208:211], v[168:171]
	s_waitcnt lgkmcnt(5)
	v_mfma_f32_16x16x32_f16 v[172:175], v[126:129], v[212:215], v[172:175]
	s_waitcnt lgkmcnt(4)
	v_mfma_f32_16x16x32_f16 v[50:53], v[126:129], v[216:219], v[50:53]
	s_waitcnt vmcnt(14)
	v_mfma_f32_16x16x32_f16 v[58:61], v[136:139], v[200:203], v[58:61]
	v_mfma_f32_16x16x32_f16 v[66:69], v[136:139], v[208:211], v[66:69]
	v_mfma_f32_16x16x32_f16 v[78:81], v[136:139], v[212:215], v[78:81]
	v_mfma_f32_16x16x32_f16 v[70:73], v[136:139], v[216:219], v[70:73]
	s_waitcnt vmcnt(13)
	v_mfma_f32_16x16x32_f16 v[54:57], v[184:187], v[200:203], v[54:57]
	v_mfma_f32_16x16x32_f16 v[74:77], v[184:187], v[208:211], v[74:77]
	v_mfma_f32_16x16x32_f16 v[82:85], v[184:187], v[212:215], v[82:85]
	v_mfma_f32_16x16x32_f16 v[62:65], v[184:187], v[216:219], v[62:65]
	s_waitcnt vmcnt(12)
	v_mfma_f32_16x16x32_f16 v[38:41], v[204:207], v[200:203], v[38:41]
	buffer_load_dwordx4 v[126:129], v147, s[16:19], s8 offen
	buffer_load_dwordx4 v[136:139], v148, s[16:19], s8 offen
	buffer_load_dwordx4 v[184:187], v149, s[16:19], s8 offen
	buffer_load_dwordx4 v[200:203], v150, s[16:19], s8 offen
	v_mfma_f32_16x16x32_f16 v[42:45], v[204:207], v[208:211], v[42:45]
	v_mfma_f32_16x16x32_f16 v[46:49], v[204:207], v[212:215], v[46:49]
	v_mfma_f32_16x16x32_f16 v[34:37], v[204:207], v[216:219], v[34:37]
	v_add_u32_e32 v111, s76, v111
	ds_read_b128 v[204:207], v111
	ds_read_b128 v[208:211], v111 offset:16384
	ds_read_b128 v[212:215], v111 offset:32768
	ds_read_b128 v[216:219], v111 offset:49152
	s_add_i32 s8, s22, s45
	s_waitcnt vmcnt(15) lgkmcnt(7)
	v_mfma_f32_16x16x32_f16 v[164:167], v[94:97], v[176:179], v[164:167]
	s_waitcnt lgkmcnt(6)
	v_mfma_f32_16x16x32_f16 v[168:171], v[94:97], v[220:223], v[168:171]
	s_waitcnt vmcnt(14)
	v_mfma_f32_16x16x32_f16 v[58:61], v[122:125], v[176:179], v[58:61]
	v_mfma_f32_16x16x32_f16 v[66:69], v[122:125], v[220:223], v[66:69]
	s_waitcnt lgkmcnt(5)
	v_mfma_f32_16x16x32_f16 v[78:81], v[122:125], v[224:227], v[78:81]
	s_waitcnt lgkmcnt(4)
	v_mfma_f32_16x16x32_f16 v[70:73], v[122:125], v[228:231], v[70:73]
	s_waitcnt vmcnt(13)
	v_mfma_f32_16x16x32_f16 v[54:57], v[156:159], v[176:179], v[54:57]
	v_mfma_f32_16x16x32_f16 v[74:77], v[156:159], v[220:223], v[74:77]
	v_mfma_f32_16x16x32_f16 v[82:85], v[156:159], v[224:227], v[82:85]
	v_mfma_f32_16x16x32_f16 v[62:65], v[156:159], v[228:231], v[62:65]
	s_waitcnt vmcnt(12)
	v_mfma_f32_16x16x32_f16 v[38:41], v[180:183], v[176:179], v[38:41]
	v_mfma_f32_16x16x32_f16 v[42:45], v[180:183], v[220:223], v[42:45]
	buffer_load_dwordx4 v[122:125], v147, s[16:19], s8 offen
	buffer_load_dwordx4 v[156:159], v148, s[16:19], s8 offen
	buffer_load_dwordx4 v[176:179], v149, s[16:19], s8 offen
	buffer_load_dwordx4 v[220:223], v150, s[16:19], s8 offen
	v_mfma_f32_16x16x32_f16 v[50:53], v[94:97], v[228:231], v[50:53]
	v_mfma_f32_16x16x32_f16 v[46:49], v[180:183], v[224:227], v[46:49]
	v_mfma_f32_16x16x32_f16 v[34:37], v[180:183], v[228:231], v[34:37]
	v_mfma_f32_16x16x32_f16 v[172:175], v[94:97], v[224:227], v[172:175]
	v_add_u32_e32 v98, s77, v98
	ds_read_b128 v[94:97], v98
	ds_read_b128 v[180:183], v98 offset:16384
	ds_read_b128 v[224:227], v98 offset:32768
	ds_read_b128 v[228:231], v98 offset:49152
	s_add_i32 s8, s22, s46
	s_waitcnt vmcnt(15) lgkmcnt(7)
	v_mfma_f32_16x16x32_f16 v[164:167], v[90:93], v[204:207], v[164:167]
	s_waitcnt lgkmcnt(6)
	v_mfma_f32_16x16x32_f16 v[168:171], v[90:93], v[208:211], v[168:171]
	s_waitcnt lgkmcnt(5)
	v_mfma_f32_16x16x32_f16 v[172:175], v[90:93], v[212:215], v[172:175]
	s_waitcnt lgkmcnt(4)
	v_mfma_f32_16x16x32_f16 v[90:93], v[90:93], v[216:219], v[50:53]
	s_waitcnt vmcnt(14)
	v_mfma_f32_16x16x32_f16 v[232:235], v[188:191], v[204:207], v[58:61]
	v_mfma_f32_16x16x32_f16 v[66:69], v[188:191], v[208:211], v[66:69]
	v_mfma_f32_16x16x32_f16 v[78:81], v[188:191], v[212:215], v[78:81]
	v_mfma_f32_16x16x32_f16 v[70:73], v[188:191], v[216:219], v[70:73]
	s_waitcnt vmcnt(13)
	v_mfma_f32_16x16x32_f16 v[188:191], v[192:195], v[204:207], v[54:57]
	v_mfma_f32_16x16x32_f16 v[74:77], v[192:195], v[208:211], v[74:77]
	v_mfma_f32_16x16x32_f16 v[82:85], v[192:195], v[212:215], v[82:85]
	v_mfma_f32_16x16x32_f16 v[62:65], v[192:195], v[216:219], v[62:65]
	s_waitcnt vmcnt(12)
	v_mfma_f32_16x16x32_f16 v[192:195], v[196:199], v[204:207], v[38:41]
	buffer_load_dwordx4 v[58:61], v147, s[16:19], s8 offen
	buffer_load_dwordx4 v[54:57], v148, s[16:19], s8 offen
	buffer_load_dwordx4 v[50:53], v149, s[16:19], s8 offen
	buffer_load_dwordx4 v[38:41], v150, s[16:19], s8 offen
	v_mfma_f32_16x16x32_f16 v[42:45], v[196:199], v[208:211], v[42:45]
	v_mfma_f32_16x16x32_f16 v[46:49], v[196:199], v[212:215], v[46:49]
	v_mfma_f32_16x16x32_f16 v[196:199], v[196:199], v[216:219], v[34:37]
	v_add_u32_e32 v99, s78, v99
	ds_read_b128 v[204:207], v99
	ds_read_b128 v[208:211], v99 offset:16384
	ds_read_b128 v[212:215], v99 offset:32768
	ds_read_b128 v[216:219], v99 offset:49152
	s_add_i32 s8, s22, s47
	s_waitcnt vmcnt(15) lgkmcnt(7)
	v_mfma_f32_16x16x32_f16 v[164:167], v[86:89], v[94:97], v[164:167]
	s_waitcnt lgkmcnt(6)
	v_mfma_f32_16x16x32_f16 v[168:171], v[86:89], v[180:183], v[168:171]
	s_waitcnt lgkmcnt(5)
	v_mfma_f32_16x16x32_f16 v[172:175], v[86:89], v[224:227], v[172:175]
	s_waitcnt lgkmcnt(4)
	v_mfma_f32_16x16x32_f16 v[86:89], v[86:89], v[228:231], v[90:93]
	s_waitcnt vmcnt(14)
	v_mfma_f32_16x16x32_f16 v[232:235], v[140:143], v[94:97], v[232:235]
	v_mfma_f32_16x16x32_f16 v[66:69], v[140:143], v[180:183], v[66:69]
	v_mfma_f32_16x16x32_f16 v[236:239], v[140:143], v[224:227], v[78:81]
	v_mfma_f32_16x16x32_f16 v[70:73], v[140:143], v[228:231], v[70:73]
	s_waitcnt vmcnt(13)
	v_mfma_f32_16x16x32_f16 v[140:143], v[152:155], v[94:97], v[188:191]
	v_mfma_f32_16x16x32_f16 v[74:77], v[152:155], v[180:183], v[74:77]
	v_mfma_f32_16x16x32_f16 v[82:85], v[152:155], v[224:227], v[82:85]
	v_mfma_f32_16x16x32_f16 v[62:65], v[152:155], v[228:231], v[62:65]
	s_waitcnt vmcnt(12)
	v_mfma_f32_16x16x32_f16 v[152:155], v[160:163], v[94:97], v[192:195]
	buffer_load_dwordx4 v[94:97], v147, s[16:19], s8 offen
	buffer_load_dwordx4 v[90:93], v148, s[16:19], s8 offen
	buffer_load_dwordx4 v[78:81], v149, s[16:19], s8 offen
	buffer_load_dwordx4 v[34:37], v150, s[16:19], s8 offen
	v_mfma_f32_16x16x32_f16 v[42:45], v[160:163], v[180:183], v[42:45]
	v_mfma_f32_16x16x32_f16 v[46:49], v[160:163], v[224:227], v[46:49]
	v_mfma_f32_16x16x32_f16 v[160:163], v[160:163], v[228:231], v[196:199]
	v_add_u32_e32 v100, s79, v100
	ds_read_b128 v[180:183], v100
	ds_read_b128 v[188:191], v100 offset:16384
	ds_read_b128 v[192:195], v100 offset:32768
	ds_read_b128 v[196:199], v100 offset:49152
	s_add_i32 s8, s22, s48
	s_waitcnt vmcnt(15) lgkmcnt(7)
	v_mfma_f32_16x16x32_f16 v[164:167], v[126:129], v[204:207], v[164:167]
	s_waitcnt lgkmcnt(6)
	v_mfma_f32_16x16x32_f16 v[168:171], v[126:129], v[208:211], v[168:171]
	s_waitcnt lgkmcnt(5)
	v_mfma_f32_16x16x32_f16 v[172:175], v[126:129], v[212:215], v[172:175]
	s_waitcnt lgkmcnt(4)
	v_mfma_f32_16x16x32_f16 v[86:89], v[126:129], v[216:219], v[86:89]
	s_waitcnt vmcnt(14)
	v_mfma_f32_16x16x32_f16 v[126:129], v[136:139], v[204:207], v[232:235]
	v_mfma_f32_16x16x32_f16 v[66:69], v[136:139], v[208:211], v[66:69]
	v_mfma_f32_16x16x32_f16 v[224:227], v[136:139], v[212:215], v[236:239]
	v_mfma_f32_16x16x32_f16 v[136:139], v[136:139], v[216:219], v[70:73]
	s_waitcnt vmcnt(13)
	v_mfma_f32_16x16x32_f16 v[140:143], v[184:187], v[204:207], v[140:143]
	v_mfma_f32_16x16x32_f16 v[74:77], v[184:187], v[208:211], v[74:77]
	v_mfma_f32_16x16x32_f16 v[228:231], v[184:187], v[212:215], v[82:85]
	v_mfma_f32_16x16x32_f16 v[184:187], v[184:187], v[216:219], v[62:65]
	s_waitcnt vmcnt(12)
	v_mfma_f32_16x16x32_f16 v[152:155], v[200:203], v[204:207], v[152:155]
	v_mfma_f32_16x16x32_f16 v[204:207], v[200:203], v[208:211], v[42:45]
	buffer_load_dwordx4 v[82:85], v147, s[16:19], s8 offen
	buffer_load_dwordx4 v[70:73], v148, s[16:19], s8 offen
	buffer_load_dwordx4 v[62:65], v149, s[16:19], s8 offen
	buffer_load_dwordx4 v[42:45], v150, s[16:19], s8 offen
	v_mfma_f32_16x16x32_f16 v[46:49], v[200:203], v[212:215], v[46:49]
	v_mfma_f32_16x16x32_f16 v[160:163], v[200:203], v[216:219], v[160:163]
	v_add_u32_e32 v0, 0x1ac00, v104
	ds_read_b128 v[240:243], v0
	ds_read_b128 v[244:247], v0 offset:16
	s_waitcnt vmcnt(12) lgkmcnt(5)
	v_mfma_f32_16x16x32_f16 v[164:167], v[122:125], v[180:183], v[164:167]
	v_mfma_f32_16x16x32_f16 v[126:129], v[156:159], v[180:183], v[126:129]
	v_mfma_f32_16x16x32_f16 v[140:143], v[176:179], v[180:183], v[140:143]
	v_mfma_f32_16x16x32_f16 v[152:155], v[220:223], v[180:183], v[152:155]
	s_waitcnt lgkmcnt(4)
	v_mfma_f32_16x16x32_f16 v[168:171], v[122:125], v[188:191], v[168:171]
	v_mfma_f32_16x16x32_f16 v[208:211], v[156:159], v[188:191], v[66:69]
	v_mfma_f32_16x16x32_f16 v[212:215], v[176:179], v[188:191], v[74:77]
	v_mfma_f32_16x16x32_f16 v[204:207], v[220:223], v[188:191], v[204:207]
	s_waitcnt lgkmcnt(3)
	v_mfma_f32_16x16x32_f16 v[172:175], v[122:125], v[192:195], v[172:175]
	v_cvt_pk_f16_f32 v232, v164, v165
	v_cvt_pk_f16_f32 v233, v166, v167
	v_pk_max_f16 v232, v232, 0
	v_pk_max_f16 v233, v233, 0
	v_mfma_f32_16x16x32_f16 v[224:227], v[156:159], v[192:195], v[224:227]
	v_cvt_pk_f16_f32 v234, v126, v127
	v_cvt_pk_f16_f32 v235, v128, v129
	v_pk_max_f16 v234, v234, 0
	v_pk_max_f16 v235, v235, 0
	v_mfma_f32_16x16x32_f16 v[228:231], v[176:179], v[192:195], v[228:231]
	v_cvt_pk_f16_f32 v236, v140, v141
	v_cvt_pk_f16_f32 v237, v142, v143
	v_pk_max_f16 v236, v236, 0
	v_pk_max_f16 v237, v237, 0
	v_mfma_f32_16x16x32_f16 v[216:219], v[220:223], v[192:195], v[46:49]
	v_cvt_pk_f16_f32 v238, v152, v153
	v_cvt_pk_f16_f32 v239, v154, v155
	v_pk_max_f16 v238, v238, 0
	v_pk_max_f16 v239, v239, 0
	s_waitcnt lgkmcnt(2)
	v_mfma_f32_16x16x32_f16 v[200:203], v[122:125], v[196:199], v[86:89]
	v_cvt_pk_f16_f32 v180, v168, v169
	v_cvt_pk_f16_f32 v181, v170, v171
	v_pk_max_f16 v180, v180, 0
	v_pk_max_f16 v181, v181, 0
	s_add_i32 s8, s22, s49
	buffer_load_dwordx4 v[86:89], v147, s[16:19], s8 offen
	buffer_load_dwordx4 v[74:77], v148, s[16:19], s8 offen
	buffer_load_dwordx4 v[66:69], v149, s[16:19], s8 offen
	buffer_load_dwordx4 v[46:49], v150, s[16:19], s8 offen
	v_mfma_f32_16x16x32_f16 v[136:139], v[156:159], v[196:199], v[136:139]
	v_cvt_pk_f16_f32 v182, v208, v209
	v_cvt_pk_f16_f32 v183, v210, v211
	v_pk_max_f16 v182, v182, 0
	v_pk_max_f16 v183, v183, 0
	s_waitcnt lgkmcnt(1)
	v_mfma_f32_16x16x32_f16 v[252:255], v[240:243], v[232:235], 0
	v_cvt_pk_f16_f32 v232, v172, v173
	v_cvt_pk_f16_f32 v233, v174, v175
	v_pk_max_f16 v232, v232, 0
	v_pk_max_f16 v233, v233, 0
	v_mfma_f32_16x16x32_f16 v[184:187], v[176:179], v[196:199], v[184:187]
	v_cvt_pk_f16_f32 v188, v212, v213
	v_cvt_pk_f16_f32 v189, v214, v215
	v_pk_max_f16 v188, v188, 0
	v_pk_max_f16 v189, v189, 0
	s_waitcnt lgkmcnt(0)
	v_mfma_f32_16x16x32_f16 v[252:255], v[244:247], v[236:239], v[252:255]
	ds_read_u16 v102, v114
	ds_read_u16 v103, v114 offset:512
	ds_read_u16 v115, v114 offset:1024
	ds_read_u16 v116, v114 offset:1536
	v_cvt_pk_f16_f32 v234, v224, v225
	v_cvt_pk_f16_f32 v235, v226, v227
	v_pk_max_f16 v234, v234, 0
	v_pk_max_f16 v235, v235, 0
	v_mfma_f32_16x16x32_f16 v[160:163], v[220:223], v[196:199], v[160:163]
	v_cvt_pk_f16_f32 v190, v204, v205
	v_cvt_pk_f16_f32 v191, v206, v207
	v_pk_max_f16 v190, v190, 0
	v_pk_max_f16 v191, v191, 0
	v_mfma_f32_16x16x32_f16 v[192:195], v[240:243], v[180:183], 0
	v_cvt_pk_f16_f32 v236, v228, v229
	v_cvt_pk_f16_f32 v237, v230, v231
	v_pk_max_f16 v236, v236, 0
	v_pk_max_f16 v237, v237, 0
	v_mfma_f32_16x16x32_f16 v[192:195], v[244:247], v[188:191], v[192:195]
	v_cvt_pk_f16_f32 v238, v216, v217
	v_cvt_pk_f16_f32 v239, v218, v219
	v_pk_max_f16 v238, v238, 0
	v_pk_max_f16 v239, v239, 0
	v_cvt_pk_f16_f32 v180, v200, v201
	v_cvt_pk_f16_f32 v181, v202, v203
	v_pk_max_f16 v180, v180, 0
	v_pk_max_f16 v181, v181, 0
	v_mfma_f32_16x16x32_f16 v[196:199], v[240:243], v[232:235], 0
	v_cvt_pk_f16_f32 v182, v136, v137
	v_cvt_pk_f16_f32 v183, v138, v139
	v_pk_max_f16 v182, v182, 0
	v_pk_max_f16 v183, v183, 0
	v_mfma_f32_16x16x32_f16 v[196:199], v[244:247], v[236:239], v[196:199]
	v_cvt_pk_f16_f32 v188, v184, v185
	v_cvt_pk_f16_f32 v189, v186, v187
	v_pk_max_f16 v188, v188, 0
	v_pk_max_f16 v189, v189, 0
	v_cvt_pk_f16_f32 v190, v160, v161
	v_cvt_pk_f16_f32 v191, v162, v163
	v_pk_max_f16 v190, v190, 0
	v_pk_max_f16 v191, v191, 0
	v_mfma_f32_16x16x32_f16 v[122:125], v[240:243], v[180:183], 0
	s_nop 0
	v_mfma_f32_16x16x32_f16 v[122:125], v[244:247], v[188:191], v[122:125]
	v_add_u32_e32 v145, 0x12c00, v105
	ds_read_b128 v[240:243], v145 offset:2048
	ds_read_b128 v[244:247], v145 offset:2064
	ds_read_b128 v[248:251], v145 offset:2080
	s_load_dword s30, s[12:13], 0x0
	v_cndmask_b32_e64 v0, v252, v192, s[2:3]
	ds_read_b128 v[252:255], v145 offset:2096
	v_cndmask_b32_e64 v0, v0, v196, s[0:1]
	v_cndmask_b32_e64 v0, v0, v122, s[26:27]
	ds_write_b32 v112, v0
	s_waitcnt vmcnt(16)
	v_cndmask_b32_e64 v1, v30, v134, s[0:1]
	v_bfi_b32 v30, s10, v1, v30
	v_perm_b32 v1, v22, v134, s24
	v_cndmask_b32_e64 v22, v22, v1, s[0:1]
	v_bfi_b32 v1, s10, v135, v18
	v_perm_b32 v121, v10, v135, s24
	v_cndmask_b32_e64 v18, v18, v1, s[0:1]
	v_cndmask_b32_e64 v10, v10, v121, s[0:1]
	s_add_i32 s22, s22, 0x80000
	s_add_i32 s11, s11, 1
	s_add_u32 s12, s12, 4
	s_addc_u32 s13, s13, 0
	v_add_u32_e32 v104, 0x400, v104
	v_add_u32_e32 v105, 0x800, v105
	v_add_u32_e32 v114, 2, v114
	s_cmp_eq_u32 s22, 0x898000
	s_waitcnt lgkmcnt(0)
	s_barrier
	ds_read_b128 v[232:235], v113
	ds_read_b128 v[236:239], v113 offset:1024
	s_waitcnt lgkmcnt(0)
	v_add_f32_e32 v0, v232, v233
	v_add_f32_e32 v1, v234, v235
	v_add_f32_e32 v121, v236, v237
	v_add_f32_e32 v144, v238, v239
	v_add_f32_e32 v0, v0, v1
	v_add_f32_e32 v121, v121, v144
	v_add_f32_e32 v0, v0, v121
	v_add_f32_e32 v0, s30, v0
	v_cvt_f16_f32_e32 v1, v0
	v_cvt_f16_f32_e32 v121, v0
	ds_write_b32 v106, v0
	v_add_u32_e32 v106, 4, v106
	v_permlane16_swap_b32_e32 v1, v121
	s_cbranch_scc0 .LBB1_4
